# s1_wt
# speedup vs baseline: 1.0612x; 1.0612x over previous
.LBB0_7:
	s_or_b64 exec, exec, s[4:5]
	s_mov_b32 s4, 0x46cc5e42
	v_mul_f64 v[4:5], v[8:9], v[8:9]
	v_mov_b32_e32 v18, 0x9037ab78
	v_mov_b32_e32 v19, 0x3e21eeb6
	s_mov_b32 s5, 0xbda907db
	v_mul_f64 v[12:13], v[4:5], 0.5
	v_fmac_f64_e32 v[18:19], s[4:5], v[4:5]
	v_mov_b32_e32 v20, 0xa17f65f6
	v_mov_b32_e32 v21, 0xbe927e4f
	v_add_f64 v[14:15], -v[12:13], 1.0
	v_fmac_f64_e32 v[20:21], v[4:5], v[18:19]
	v_mov_b32_e32 v18, 0x19f4ec90
	v_mov_b32_e32 v19, 0x3efa01a0
	v_add_f64 v[16:17], -v[14:15], 1.0
	v_fmac_f64_e32 v[18:19], v[4:5], v[20:21]
	v_mov_b32_e32 v20, 0x16c16967
	v_mov_b32_e32 v21, 0xbf56c16c
	v_add_f64 v[12:13], v[16:17], -v[12:13]
	v_fmac_f64_e32 v[20:21], v[4:5], v[18:19]
	v_mov_b32_e32 v18, 0x55555555
	v_mov_b32_e32 v19, 0x3fa55555
	v_mul_f64 v[16:17], v[4:5], v[4:5]
	v_fmac_f64_e32 v[18:19], v[4:5], v[20:21]
	v_fma_f64 v[12:13], v[8:9], -v[10:11], v[12:13]
	v_fmac_f64_e32 v[12:13], v[16:17], v[18:19]
	s_mov_b32 s6, 0xf9a43bb8
	v_add_f64 v[12:13], v[14:15], v[12:13]
	v_mov_b32_e32 v14, 0xb42fdfa7
	v_mov_b32_e32 v15, 0xbe5ae600
	s_mov_b32 s7, 0x3de5e0b2
	v_fmac_f64_e32 v[14:15], s[6:7], v[4:5]
	v_mov_b32_e32 v16, 0x796cde01
	v_mov_b32_e32 v17, 0x3ec71de3
	v_fmac_f64_e32 v[16:17], v[4:5], v[14:15]
	v_mov_b32_e32 v14, 0x19e83e5c
	v_mov_b32_e32 v15, 0xbf2a01a0
	v_fmac_f64_e32 v[14:15], v[4:5], v[16:17]
	v_mov_b32_e32 v16, 0x11110bb3
	v_mov_b32_e32 v17, 0x3f811111
	v_fmac_f64_e32 v[16:17], v[4:5], v[14:15]
	v_mul_f64 v[14:15], v[8:9], -v[4:5]
	v_mul_f64 v[18:19], v[10:11], 0.5
	s_mov_b32 s4, 0x55555555
	v_fmac_f64_e32 v[18:19], v[14:15], v[16:17]
	s_mov_b32 s5, 0xbfc55555
	v_fma_f64 v[4:5], v[4:5], v[18:19], -v[10:11]
	v_fmac_f64_e32 v[4:5], s[4:5], v[14:15]
	v_lshlrev_b32_e32 v1, 30, v3
	v_and_b32_e32 v3, 1, v3
	v_add_f64 v[4:5], v[8:9], -v[4:5]
	v_cmp_eq_u32_e32 vcc, 0, v3
	v_xor_b32_e32 v9, v1, v7
	s_brev_b32 s3, 1
	v_cndmask_b32_e32 v8, v13, v5, vcc
	v_xor_b32_e32 v5, 0x80000000, v5
	v_cndmask_b32_e32 v5, v5, v13, vcc
	v_bitop3_b32 v8, v8, v9, s3 bitop3:0x78
	v_bitop3_b32 v1, v5, v1, s3 bitop3:0x78
	s_movk_i32 s3, 0x1f8
	v_cndmask_b32_e32 v3, v12, v4, vcc
	v_cndmask_b32_e32 v4, v4, v12, vcc
	v_cmp_class_f64_e64 vcc, v[6:7], s3
	v_mov_b32_e32 v7, 0x7ff80000
	s_nop 0
	v_cndmask_b32_e32 v4, 0, v4, vcc
	v_cndmask_b32_e32 v5, v7, v1, vcc
	v_cndmask_b32_e32 v6, 0, v3, vcc
	v_cndmask_b32_e32 v7, v7, v8, vcc
	v_ashrrev_i32_e32 v3, 31, v2
	s_waitcnt lgkmcnt(0)
	v_lshl_add_u64 v[2:3], v[2:3], 3, s[8:9]
	v_cvt_f32_f64_e32 v4, v[4:5]
	v_cvt_f32_f64_e32 v5, v[6:7]
	global_store_dwordx2 v[2:3], v[4:5], off sc0 sc1
	s_branch .LBB0_2

.Lprep_go:
	s_lshl_b32 s27, s23, 12
	s_lshl_b32 s28, s22, 7
	s_add_i32 s27, s27, s28
	s_add_u32 s0, s0, s27
	s_addc_u32 s1, s1, 0
	global_load_dwordx4 v[8:11], v3, s[0:1] nt
	global_load_dwordx4 v[12:15], v3, s[0:1] offset:16 nt
	global_load_dwordx4 v[16:19], v3, s[0:1] offset:128 nt
	global_load_dwordx4 v[20:23], v3, s[0:1] offset:144 nt
	global_load_dwordx4 v[24:27], v3, s[0:1] offset:256 nt
	global_load_dwordx4 v[28:31], v3, s[0:1] offset:272 nt
	global_load_dwordx4 v[32:35], v3, s[0:1] offset:384 nt
	global_load_dwordx4 v[36:39], v3, s[0:1] offset:400 nt
	s_mul_i32 s27, s22, s25
	s_lshl_b32 s28, s24, 6
	s_add_i32 s27, s27, s28
	s_add_u32 s2, s2, s27
	s_addc_u32 s3, s3, 0
	s_add_u32 s4, s2, s25
	s_addc_u32 s5, s3, 0
	s_add_u32 s6, s4, s25
	s_addc_u32 s7, s5, 0
	s_add_u32 s8, s6, s25
	s_addc_u32 s9, s7, 0
	s_waitcnt vmcnt(6)
	v_cvt_pk_f16_f32 v8, v8, v9
	v_cvt_pk_f16_f32 v9, v10, v11
	v_cvt_pk_f16_f32 v10, v12, v13
	v_cvt_pk_f16_f32 v11, v14, v15
	global_store_dwordx4 v4, v[8:11], s[2:3] sc0 sc1
	s_waitcnt vmcnt(5)
	v_cvt_pk_f16_f32 v16, v16, v17
	v_cvt_pk_f16_f32 v17, v18, v19
	v_cvt_pk_f16_f32 v18, v20, v21
	v_cvt_pk_f16_f32 v19, v22, v23
	global_store_dwordx4 v4, v[16:19], s[4:5] sc0 sc1
	s_waitcnt vmcnt(4)
	v_cvt_pk_f16_f32 v24, v24, v25
	v_cvt_pk_f16_f32 v25, v26, v27
	v_cvt_pk_f16_f32 v26, v28, v29
	v_cvt_pk_f16_f32 v27, v30, v31
	global_store_dwordx4 v4, v[24:27], s[6:7] sc0 sc1
	s_waitcnt vmcnt(3)
	v_cvt_pk_f16_f32 v32, v32, v33
	v_cvt_pk_f16_f32 v33, v34, v35
	v_cvt_pk_f16_f32 v34, v36, v37
	v_cvt_pk_f16_f32 v35, v38, v39
	global_store_dwordx4 v4, v[32:35], s[8:9] sc0 sc1
	s_endpgm

.LBB1_34:
	v_add_u32_e32 v88, s41, v240
	ds_read_b64_tr_b16 v[80:81], v88 offset:24576
	ds_read_b64_tr_b16 v[82:83], v88 offset:25088
	v_cvt_pk_f16_f32 v64, v64, v65
	v_cvt_pk_f16_f32 v65, v66, v67
	v_cvt_pk_f16_f32 v66, v68, v69
	v_cvt_pk_f16_f32 v67, v70, v71
	ds_read_b64_tr_b16 v[68:69], v88 offset:25600
	ds_read_b64_tr_b16 v[70:71], v88 offset:26112
	s_waitcnt lgkmcnt(2)
	v_mfma_f32_32x32x16_f16 v[0:15], v[64:67], v[80:83], v[0:15]
	ds_read_b64_tr_b16 v[80:81], v88 offset:28672
	ds_read_b64_tr_b16 v[82:83], v88 offset:29184
	ds_read_b64_tr_b16 v[84:85], v88 offset:29696
	ds_read_b64_tr_b16 v[86:87], v88 offset:30208
	v_cvt_pk_f16_f32 v72, v72, v73
	v_cvt_pk_f16_f32 v73, v74, v75
	v_cvt_pk_f16_f32 v74, v76, v77
	v_cvt_pk_f16_f32 v75, v78, v79
	v_cvt_pk_f16_f32 v48, v48, v49
	v_cvt_pk_f16_f32 v49, v50, v51
	s_waitcnt lgkmcnt(2)
	v_mfma_f32_32x32x16_f16 v[16:31], v[64:67], v[80:83], v[16:31]
	v_cvt_pk_f16_f32 v50, v52, v53
	v_cvt_pk_f16_f32 v51, v54, v55
	v_cvt_pk_f16_f32 v52, v56, v57
	v_cvt_pk_f16_f32 v53, v58, v59
	v_cvt_pk_f16_f32 v54, v60, v61
	v_cvt_pk_f16_f32 v55, v62, v63
	ds_read_b64_tr_b16 v[56:57], v88 offset:26624
	ds_read_b64_tr_b16 v[58:59], v88 offset:27136
	ds_read_b64_tr_b16 v[60:61], v88 offset:27648
	ds_read_b64_tr_b16 v[62:63], v88 offset:28160
	v_mfma_f32_32x32x16_f16 v[0:15], v[72:75], v[68:71], v[0:15]
	v_pk_add_f16 v64, v64, v72
	v_pk_add_f16 v65, v65, v73
	v_pk_add_f16 v66, v66, v74
	v_pk_add_f16 v67, v67, v75
	v_pk_add_f16 v68, v48, v52
	s_lshl_b64 s[0:1], s[4:5], 1
	s_add_u32 s0, s10, s0
	s_waitcnt lgkmcnt(2)
	v_mfma_f32_32x32x16_f16 v[0:15], v[48:51], v[56:59], v[0:15]
	v_pk_add_f16 v56, v49, v53
	v_pk_add_f16 v57, v50, v54
	v_pk_add_f16 v58, v51, v55
	s_addc_u32 s1, s11, s1
	v_pk_add_f16 v59, v67, v58
	v_pk_add_f16 v58, v66, v57
	v_pk_add_f16 v57, v65, v56
	v_mfma_f32_32x32x16_f16 v[16:31], v[72:75], v[84:87], v[16:31]
	v_pk_add_f16 v56, v64, v68
	s_lshl_b32 s2, s33, 12
	s_add_i32 s2, s2, 0
	s_lshl_b32 s3, s36, 1
	s_add_u32 s0, s0, s3
	s_addc_u32 s1, s1, 0
	v_mfma_f32_32x32x16_f16 v[32:47], v[56:59], v[128:131], v[32:47]
	ds_read_b64_tr_b16 v[56:57], v88 offset:30720
	ds_read_b64_tr_b16 v[58:59], v88 offset:31232
	ds_read_b64_tr_b16 v[64:65], v88 offset:31744
	ds_read_b64_tr_b16 v[66:67], v88 offset:32256
	s_waitcnt lgkmcnt(2)
	v_mfma_f32_32x32x16_f16 v[16:31], v[48:51], v[56:59], v[16:31]
	s_nop 5
	v_rcp_f32_e32 v32, v32
	v_rcp_f32_e32 v33, v33
	v_lshl_add_u32 v48, v238, 1, s2
	v_lshlrev_b32_e32 v49, 7, v239
	v_rcp_f32_e32 v34, v34
	v_add_u32_e32 v50, v48, v49
	v_rcp_f32_e32 v35, v35
	v_mfma_f32_32x32x16_f16 v[0:15], v[52:55], v[60:63], v[0:15]
	v_rcp_f32_e32 v36, v36
	v_rcp_f32_e32 v37, v37
	v_rcp_f32_e32 v38, v38
	v_rcp_f32_e32 v39, v39
	v_rcp_f32_e32 v40, v40
	v_rcp_f32_e32 v41, v41
	v_rcp_f32_e32 v42, v42
	s_waitcnt lgkmcnt(0)
	v_mfma_f32_32x32x16_f16 v[16:31], v[52:55], v[64:67], v[16:31]
	s_nop 2
	v_fma_mixlo_f16 v0, v0, v32, 0
	ds_write_b16 v50, v0 offset:50176
	v_rcp_f32_e32 v43, v43
	v_rcp_f32_e32 v44, v44
	v_rcp_f32_e32 v45, v45
	v_rcp_f32_e32 v46, v46
	v_rcp_f32_e32 v47, v47
	s_nop 1
	v_fma_mixlo_f16 v0, v16, v32, 0
	ds_write_b16 v50, v0 offset:50240
	v_fma_mixlo_f16 v0, v1, v33, 0
	ds_write_b16 v50, v0 offset:50304
	v_fma_mixlo_f16 v0, v17, v33, 0
	ds_write_b16 v50, v0 offset:50368
	v_fma_mixlo_f16 v0, v2, v34, 0
	ds_write_b16 v50, v0 offset:50432
	v_fma_mixlo_f16 v0, v18, v34, 0
	ds_write_b16 v50, v0 offset:50496
	v_fma_mixlo_f16 v0, v3, v35, 0
	ds_write_b16 v50, v0 offset:50560
	v_fma_mixlo_f16 v0, v19, v35, 0
	ds_write_b16 v50, v0 offset:50624
	v_or_b32_e32 v0, 0x400, v49
	v_add_u32_e32 v0, v48, v0
	v_fma_mixlo_f16 v1, v4, v36, 0
	ds_write_b16 v0, v1 offset:50176
	v_fma_mixlo_f16 v1, v20, v36, 0
	ds_write_b16 v0, v1 offset:50240
	v_or_b32_e32 v0, 0x480, v49
	v_add_u32_e32 v0, v48, v0
	v_fma_mixlo_f16 v1, v5, v37, 0
	ds_write_b16 v0, v1 offset:50176
	v_fma_mixlo_f16 v1, v21, v37, 0
	ds_write_b16 v0, v1 offset:50240
	v_or_b32_e32 v0, 0x500, v49
	v_add_u32_e32 v0, v48, v0
	v_fma_mixlo_f16 v1, v6, v38, 0
	ds_write_b16 v0, v1 offset:50176
	v_fma_mixlo_f16 v1, v22, v38, 0
	ds_write_b16 v0, v1 offset:50240
	v_or_b32_e32 v0, 0x580, v49
	v_add_u32_e32 v0, v48, v0
	v_fma_mixlo_f16 v1, v7, v39, 0
	ds_write_b16 v0, v1 offset:50176
	v_fma_mixlo_f16 v1, v23, v39, 0
	ds_write_b16 v0, v1 offset:50240
	v_or_b32_e32 v0, 0x800, v49
	v_add_u32_e32 v0, v48, v0
	v_fma_mixlo_f16 v1, v8, v40, 0
	ds_write_b16 v0, v1 offset:50176
	v_fma_mixlo_f16 v1, v24, v40, 0
	ds_write_b16 v0, v1 offset:50240
	v_or_b32_e32 v0, 0x880, v49
	v_add_u32_e32 v0, v48, v0
	v_fma_mixlo_f16 v1, v9, v41, 0
	ds_write_b16 v0, v1 offset:50176
	v_fma_mixlo_f16 v1, v25, v41, 0
	ds_write_b16 v0, v1 offset:50240
	v_or_b32_e32 v0, 0x900, v49
	v_add_u32_e32 v0, v48, v0
	v_fma_mixlo_f16 v1, v10, v42, 0
	ds_write_b16 v0, v1 offset:50176
	v_fma_mixlo_f16 v1, v26, v42, 0
	ds_write_b16 v0, v1 offset:50240
	v_or_b32_e32 v0, 0x980, v49
	v_add_u32_e32 v0, v48, v0
	v_fma_mixlo_f16 v1, v11, v43, 0
	ds_write_b16 v0, v1 offset:50176
	v_fma_mixlo_f16 v1, v27, v43, 0
	ds_write_b16 v0, v1 offset:50240
	v_or_b32_e32 v0, 0xc00, v49
	v_add_u32_e32 v0, v48, v0
	v_fma_mixlo_f16 v1, v12, v44, 0
	ds_write_b16 v0, v1 offset:50176
	v_fma_mixlo_f16 v1, v28, v44, 0
	ds_write_b16 v0, v1 offset:50240
	v_or_b32_e32 v0, 0xc80, v49
	v_add_u32_e32 v0, v48, v0
	v_fma_mixlo_f16 v1, v13, v45, 0
	ds_write_b16 v0, v1 offset:50176
	v_fma_mixlo_f16 v1, v29, v45, 0
	ds_write_b16 v0, v1 offset:50240
	v_or_b32_e32 v0, 0xd00, v49
	v_add_u32_e32 v0, v48, v0
	v_fma_mixlo_f16 v1, v14, v46, 0
	ds_write_b16 v0, v1 offset:50176
	v_fma_mixlo_f16 v1, v30, v46, 0
	ds_write_b16 v0, v1 offset:50240
	v_or_b32_e32 v0, 0xd80, v49
	v_add_u32_e32 v0, v48, v0
	v_fma_mixlo_f16 v1, v15, v47, 0
	ds_write_b16 v0, v1 offset:50176
	v_fma_mixlo_f16 v1, v31, v47, 0
	ds_write_b16 v0, v1 offset:50240
	v_and_b32_e32 v0, 56, v237
	v_lshlrev_b32_e32 v8, 1, v0
	v_lshrrev_b32_e32 v14, 3, v236
	v_add_u32_e32 v15, s2, v8
	s_waitcnt lgkmcnt(0)
	v_lshl_add_u32 v0, v14, 7, v15
	v_or_b32_e32 v16, 8, v14
	ds_read_b128 v[0:3], v0 offset:50176
	v_lshl_add_u32 v4, v16, 7, v15
	ds_read_b128 v[4:7], v4 offset:50176
	v_mov_b32_e32 v9, 0
	v_lshl_add_u64 v[10:11], s[0:1], 0, v[8:9]
	v_lshlrev_b32_e32 v8, 11, v14
	v_lshl_add_u64 v[12:13], v[10:11], 0, v[8:9]
	v_lshlrev_b32_e32 v8, 11, v16
	s_waitcnt lgkmcnt(1)
	global_store_dwordx4 v[12:13], v[0:3], off sc0 sc1
	s_nop 1
	v_lshl_add_u64 v[0:1], v[10:11], 0, v[8:9]
	s_waitcnt lgkmcnt(0)
	global_store_dwordx4 v[0:1], v[4:7], off sc0 sc1
	s_nop 1
	v_or_b32_e32 v4, 16, v14
	v_lshl_add_u32 v0, v4, 7, v15
	v_or_b32_e32 v14, 24, v14
	ds_read_b128 v[0:3], v0 offset:50176
	v_lshlrev_b32_e32 v8, 11, v4
	v_lshl_add_u32 v4, v14, 7, v15
	ds_read_b128 v[4:7], v4 offset:50176
	v_lshl_add_u64 v[12:13], v[10:11], 0, v[8:9]
	v_lshlrev_b32_e32 v8, 11, v14
	s_waitcnt lgkmcnt(1)
	global_store_dwordx4 v[12:13], v[0:3], off sc0 sc1
	s_nop 1
	v_lshl_add_u64 v[0:1], v[10:11], 0, v[8:9]
	s_waitcnt lgkmcnt(0)
	global_store_dwordx4 v[0:1], v[4:7], off sc0 sc1
	s_waitcnt lgkmcnt(0)
	s_barrier
	s_endpgm

.Lepi_d0:
	s_waitcnt vmcnt(0)
	s_lshl_b32 s35, s29, 11
	v_add_u32_e32 v104, 0x8000, v0
	v_add_u32_e32 v105, 0x10000, v0
	v_add_u32_e32 v106, 0x18000, v0
	s_add_i32 s31, s34, 0
	s_lshr_b32 s30, s31, 10
	s_and_b32 s31, s31, 0x3ff
	s_lshl_b32 s31, s31, 1
	s_cmp_eq_u32 s30, 1
	s_cselect_b64 s[44:45], s[16:17], s[14:15]
	s_cmp_eq_u32 s30, 2
	s_cselect_b64 s[44:45], s[18:19], s[44:45]
	s_add_u32 s44, s44, s31
	s_addc_u32 s45, s45, 0
	s_add_u32 s44, s44, s35
	s_addc_u32 s45, s45, 0
	s_add_i32 s31, s34, 32
	s_lshr_b32 s30, s31, 10
	s_and_b32 s31, s31, 0x3ff
	s_lshl_b32 s31, s31, 1
	s_cmp_eq_u32 s30, 1
	s_cselect_b64 s[46:47], s[16:17], s[14:15]
	s_cmp_eq_u32 s30, 2
	s_cselect_b64 s[46:47], s[18:19], s[46:47]
	s_add_u32 s46, s46, s31
	s_addc_u32 s47, s47, 0
	s_add_u32 s46, s46, s35
	s_addc_u32 s47, s47, 0
	s_add_i32 s31, s34, 64
	s_lshr_b32 s30, s31, 10
	s_and_b32 s31, s31, 0x3ff
	s_lshl_b32 s31, s31, 1
	s_cmp_eq_u32 s30, 1
	s_cselect_b64 s[48:49], s[16:17], s[14:15]
	s_cmp_eq_u32 s30, 2
	s_cselect_b64 s[48:49], s[18:19], s[48:49]
	s_add_u32 s48, s48, s31
	s_addc_u32 s49, s49, 0
	s_add_u32 s48, s48, s35
	s_addc_u32 s49, s49, 0
	s_waitcnt lgkmcnt(0)
	ds_read_b128 v[2:5], v102 offset:0
	ds_read_b128 v[6:9], v102 offset:64
	ds_read_b128 v[10:13], v102 offset:128
	ds_read_b128 v[14:17], v102 offset:3328
	ds_read_b128 v[18:21], v102 offset:3392
	ds_read_b128 v[22:25], v102 offset:3456
	ds_read_b128 v[26:29], v102 offset:6656
	ds_read_b128 v[30:33], v102 offset:6720
	ds_read_b128 v[34:37], v102 offset:6784
	ds_read_b128 v[38:41], v102 offset:9984
	ds_read_b128 v[42:45], v102 offset:10048
	ds_read_b128 v[46:49], v102 offset:10112
	s_waitcnt lgkmcnt(11)
	global_store_dwordx4 v0, v[2:5], s[44:45] sc0 sc1
	s_waitcnt lgkmcnt(10)
	global_store_dwordx4 v0, v[6:9], s[46:47] sc0 sc1
	s_waitcnt lgkmcnt(9)
	global_store_dwordx4 v0, v[10:13], s[48:49] sc0 sc1
	s_waitcnt lgkmcnt(8)
	global_store_dwordx4 v104, v[14:17], s[44:45] sc0 sc1
	s_waitcnt lgkmcnt(7)
	global_store_dwordx4 v104, v[18:21], s[46:47] sc0 sc1
	s_waitcnt lgkmcnt(6)
	global_store_dwordx4 v104, v[22:25], s[48:49] sc0 sc1
	s_waitcnt lgkmcnt(5)
	global_store_dwordx4 v105, v[26:29], s[44:45] sc0 sc1
	s_waitcnt lgkmcnt(4)
	global_store_dwordx4 v105, v[30:33], s[46:47] sc0 sc1
	s_waitcnt lgkmcnt(3)
	global_store_dwordx4 v105, v[34:37], s[48:49] sc0 sc1
	s_waitcnt lgkmcnt(2)
	global_store_dwordx4 v106, v[38:41], s[44:45] sc0 sc1
	s_waitcnt lgkmcnt(1)
	global_store_dwordx4 v106, v[42:45], s[46:47] sc0 sc1
	s_waitcnt lgkmcnt(0)
	global_store_dwordx4 v106, v[46:49], s[48:49] sc0 sc1
	s_branch .LBB2_2

.LBB3_4:
	s_lshl_b32 s12, s8, 14
	s_add_i32 s12, s12, 0
	v_add3_u32 v42, s12, v37, v35
	v_add3_u32 v58, s12, v36, v35
	s_barrier
	ds_read_b128 v[38:41], v42 offset:8192
	ds_read_b128 v[42:45], v42 offset:9216
	ds_read_b128 v[46:49], v58
	ds_read_b128 v[50:53], v58 offset:1024
	ds_read_b128 v[54:57], v58 offset:2048
	ds_read_b128 v[58:61], v58 offset:3072
	s_waitcnt lgkmcnt(0)
	v_mfma_f32_16x16x32_f16 v[30:33], v[46:49], v[38:41], v[30:33]
	s_add_i32 s12, s8, 1
	s_cmp_lg_u32 s8, 4
	s_cselect_b32 s8, s12, 0
	v_mfma_f32_16x16x32_f16 v[22:25], v[46:49], v[42:45], v[22:25]
	s_add_i32 s11, s11, -1
	s_cmp_eq_u32 s11, 0
	v_mfma_f32_16x16x32_f16 v[26:29], v[50:53], v[38:41], v[26:29]
	v_mfma_f32_16x16x32_f16 v[14:17], v[50:53], v[42:45], v[14:17]
	v_mfma_f32_16x16x32_f16 v[18:21], v[54:57], v[38:41], v[18:21]
	v_mfma_f32_16x16x32_f16 v[6:9], v[54:57], v[42:45], v[6:9]
	v_mfma_f32_16x16x32_f16 v[10:13], v[58:61], v[38:41], v[10:13]
	v_mfma_f32_16x16x32_f16 v[2:5], v[58:61], v[42:45], v[2:5]
	s_cbranch_scc0 .LBB3_4
	s_or_b32 s8, s10, s4
	v_or_b32_e32 v35, s8, v34
	v_lshl_or_b32 v34, v1, 2, s9
	v_mov_b32_e32 v37, 0
	v_or_b32_e32 v34, s7, v34
	v_lshlrev_b32_e32 v36, 12, v35
	v_mov_b32_e32 v35, v37
	v_lshl_add_u64 v[38:39], s[2:3], 0, v[36:37]
	v_lshlrev_b64 v[40:41], 2, v[34:35]
	v_lshl_add_u64 v[42:43], v[38:39], 0, v[40:41]
	s_mov_b64 s[2:3], 0x10000
	global_store_dwordx4 v[42:43], v[10:13], off offset:192 sc0 sc1
	v_or_b32_e32 v36, 16, v34
	global_store_dwordx4 v[42:43], v[26:29], off offset:64 sc0 sc1
	v_lshl_add_u64 v[10:11], v[38:39], 0, s[2:3]
	v_lshl_add_u64 v[12:13], v[10:11], 0, v[40:41]
	v_or_b32_e32 v26, 32, v34
	v_mov_b32_e32 v27, v37
	global_store_dwordx4 v[12:13], v[22:25], off sc0 sc1
	v_lshl_add_u64 v[12:13], v[36:37], 2, v[10:11]
	global_store_dwordx4 v[42:43], v[18:21], off offset:128 sc0 sc1
	global_store_dwordx4 v[12:13], v[14:17], off sc0 sc1
	v_lshl_add_u64 v[12:13], v[26:27], 2, v[10:11]
	v_or_b32_e32 v18, 48, v34
	v_mov_b32_e32 v19, v37
	global_store_dwordx4 v[12:13], v[6:9], off sc0 sc1
	global_store_dwordx4 v[42:43], v[30:33], off sc0 sc1
	s_nop 0
	v_lshl_add_u64 v[6:7], v[18:19], 2, v[10:11]
	global_store_dwordx4 v[6:7], v[2:5], off sc0 sc1
	s_branch .LBB3_2
